# P4 o1 (P@V): transposed LDS reads of the 2nd-4th key blocks issued ahead of the first block, one LDS round trip for all four
# speedup vs baseline: 1.0111x; 1.0089x over previous
.LBB0_755:
	ds_read_b64_tr_b16 v[214:215], v165 offset:0
	ds_read_b64_tr_b16 v[216:217], v165 offset:1792
	ds_read_b64_tr_b16 v[218:219], v165 offset:32
	ds_read_b64_tr_b16 v[220:221], v165 offset:1824
	ds_read_b64_tr_b16 v[222:223], v165 offset:64
	ds_read_b64_tr_b16 v[224:225], v165 offset:1856
	ds_read_b64_tr_b16 v[226:227], v166 offset:0
	ds_read_b64_tr_b16 v[228:229], v166 offset:1792
	ds_read_b64_tr_b16 v[230:231], v166 offset:32
	ds_read_b64_tr_b16 v[232:233], v166 offset:1824
	ds_read_b64_tr_b16 v[234:235], v166 offset:64
	ds_read_b64_tr_b16 v[236:237], v166 offset:1856
	ds_read_b64_tr_b16 v[202:203], v167 offset:0
	ds_read_b64_tr_b16 v[204:205], v167 offset:1792
	ds_read_b64_tr_b16 v[206:207], v167 offset:32
	ds_read_b64_tr_b16 v[208:209], v167 offset:1824
	ds_read_b64_tr_b16 v[238:239], v167 offset:64
	ds_read_b64_tr_b16 v[240:241], v167 offset:1856
	s_and_b64 vcc, exec, s[88:89]
	s_cbranch_vccnz .LBB0_757
	ds_read_b64_tr_b16 v[78:79], v164 offset:0
	ds_read_b64_tr_b16 v[80:81], v164 offset:1792
	ds_read_b64_tr_b16 v[86:87], v164 offset:32
	ds_read_b64_tr_b16 v[88:89], v164 offset:1824
	ds_read_b64_tr_b16 v[96:97], v164 offset:64
	ds_read_b64_tr_b16 v[98:99], v164 offset:1856
	s_waitcnt lgkmcnt(0)
	s_nop 0
	v_mfma_f32_16x16x32_f16 v[78:81], v[78:81], v[70:73], 0
	v_mfma_f32_16x16x32_f16 v[86:89], v[86:89], v[70:73], 0
	v_mfma_f32_16x16x32_f16 v[70:73], v[96:99], v[70:73], 0
	s_and_b64 vcc, exec, s[90:91]
	s_cbranch_vccz .LBB0_758
	s_branch .LBB0_759

.LBB0_758:
	s_waitcnt lgkmcnt(0)
	s_nop 0
	v_mfma_f32_16x16x32_f16 v[78:81], v[214:217], v[74:77], v[78:81]
	v_mfma_f32_16x16x32_f16 v[86:89], v[218:221], v[74:77], v[86:89]
	v_mfma_f32_16x16x32_f16 v[70:73], v[222:225], v[74:77], v[70:73]
.LBB0_759:
	s_and_b64 vcc, exec, s[92:93]
	s_cbranch_vccnz .LBB0_761
	s_waitcnt lgkmcnt(0)
	s_nop 0
	v_mfma_f32_16x16x32_f16 v[78:81], v[226:229], v[82:85], v[78:81]
	v_mfma_f32_16x16x32_f16 v[86:89], v[230:233], v[82:85], v[86:89]
	v_mfma_f32_16x16x32_f16 v[70:73], v[234:237], v[82:85], v[70:73]
	s_and_b64 vcc, exec, s[94:95]
	s_cbranch_vccz .LBB0_762
	s_branch .LBB0_763

.LBB0_762:
	s_waitcnt lgkmcnt(0)
	s_nop 0
	v_mfma_f32_16x16x32_f16 v[78:81], v[202:205], v[92:95], v[78:81]
	v_mfma_f32_16x16x32_f16 v[86:89], v[206:209], v[92:95], v[86:89]
	v_mfma_f32_16x16x32_f16 v[70:73], v[238:241], v[92:95], v[70:73]

.LBB0_2167:
	ds_read_b64_tr_b16 v[214:215], v161 offset:0
	ds_read_b64_tr_b16 v[216:217], v161 offset:1792
	ds_read_b64_tr_b16 v[218:219], v161 offset:32
	ds_read_b64_tr_b16 v[220:221], v161 offset:1824
	ds_read_b64_tr_b16 v[222:223], v161 offset:64
	ds_read_b64_tr_b16 v[224:225], v161 offset:1856
	ds_read_b64_tr_b16 v[226:227], v162 offset:0
	ds_read_b64_tr_b16 v[228:229], v162 offset:1792
	ds_read_b64_tr_b16 v[230:231], v162 offset:32
	ds_read_b64_tr_b16 v[232:233], v162 offset:1824
	ds_read_b64_tr_b16 v[234:235], v162 offset:64
	ds_read_b64_tr_b16 v[236:237], v162 offset:1856
	ds_read_b64_tr_b16 v[202:203], v163 offset:0
	ds_read_b64_tr_b16 v[204:205], v163 offset:1792
	ds_read_b64_tr_b16 v[206:207], v163 offset:32
	ds_read_b64_tr_b16 v[208:209], v163 offset:1824
	ds_read_b64_tr_b16 v[238:239], v163 offset:64
	ds_read_b64_tr_b16 v[240:241], v163 offset:1856
	s_and_b64 vcc, exec, s[88:89]
	s_cbranch_vccnz .LBB0_2169
	ds_read_b64_tr_b16 v[86:87], v160 offset:0
	ds_read_b64_tr_b16 v[88:89], v160 offset:1792
	ds_read_b64_tr_b16 v[90:91], v160 offset:32
	ds_read_b64_tr_b16 v[92:93], v160 offset:1824
	ds_read_b64_tr_b16 v[94:95], v160 offset:64
	ds_read_b64_tr_b16 v[96:97], v160 offset:1856
	s_waitcnt lgkmcnt(0)
	s_nop 0
	v_mfma_f32_16x16x32_f16 v[86:89], v[86:89], v[70:73], 0
	v_mfma_f32_16x16x32_f16 v[90:93], v[90:93], v[70:73], 0
	v_mfma_f32_16x16x32_f16 v[70:73], v[94:97], v[70:73], 0
	s_and_b64 vcc, exec, s[90:91]
	s_cbranch_vccz .LBB0_2170
	s_branch .LBB0_2171

.LBB0_2170:
	s_waitcnt lgkmcnt(0)
	s_nop 0
	v_mfma_f32_16x16x32_f16 v[86:89], v[214:217], v[74:77], v[86:89]
	v_mfma_f32_16x16x32_f16 v[90:93], v[218:221], v[74:77], v[90:93]
	v_mfma_f32_16x16x32_f16 v[70:73], v[222:225], v[74:77], v[70:73]
.LBB0_2171:
	s_and_b64 vcc, exec, s[92:93]
	s_cbranch_vccnz .LBB0_2173
	s_waitcnt lgkmcnt(0)
	s_nop 0
	v_mfma_f32_16x16x32_f16 v[86:89], v[226:229], v[78:81], v[86:89]
	v_mfma_f32_16x16x32_f16 v[90:93], v[230:233], v[78:81], v[90:93]
	v_mfma_f32_16x16x32_f16 v[70:73], v[234:237], v[78:81], v[70:73]
	s_and_b64 vcc, exec, s[94:95]
	s_cbranch_vccz .LBB0_2174
	s_branch .LBB0_2175

.LBB0_2174:
	s_waitcnt lgkmcnt(0)
	s_nop 0
	v_mfma_f32_16x16x32_f16 v[86:89], v[202:205], v[82:85], v[86:89]
	v_mfma_f32_16x16x32_f16 v[90:93], v[206:209], v[82:85], v[90:93]
	v_mfma_f32_16x16x32_f16 v[70:73], v[238:241], v[82:85], v[70:73]

.LBB0_5147:
	ds_read_b64_tr_b16 v[214:215], v161 offset:0
	ds_read_b64_tr_b16 v[216:217], v161 offset:1792
	ds_read_b64_tr_b16 v[218:219], v161 offset:32
	ds_read_b64_tr_b16 v[220:221], v161 offset:1824
	ds_read_b64_tr_b16 v[222:223], v161 offset:64
	ds_read_b64_tr_b16 v[224:225], v161 offset:1856
	ds_read_b64_tr_b16 v[226:227], v162 offset:0
	ds_read_b64_tr_b16 v[228:229], v162 offset:1792
	ds_read_b64_tr_b16 v[230:231], v162 offset:32
	ds_read_b64_tr_b16 v[232:233], v162 offset:1824
	ds_read_b64_tr_b16 v[234:235], v162 offset:64
	ds_read_b64_tr_b16 v[236:237], v162 offset:1856
	ds_read_b64_tr_b16 v[202:203], v163 offset:0
	ds_read_b64_tr_b16 v[204:205], v163 offset:1792
	ds_read_b64_tr_b16 v[206:207], v163 offset:32
	ds_read_b64_tr_b16 v[208:209], v163 offset:1824
	ds_read_b64_tr_b16 v[238:239], v163 offset:64
	ds_read_b64_tr_b16 v[240:241], v163 offset:1856
	s_and_b64 vcc, exec, s[86:87]
	s_cbranch_vccnz .LBB0_5149
	ds_read_b64_tr_b16 v[86:87], v160 offset:0
	ds_read_b64_tr_b16 v[88:89], v160 offset:1792
	ds_read_b64_tr_b16 v[90:91], v160 offset:32
	ds_read_b64_tr_b16 v[92:93], v160 offset:1824
	ds_read_b64_tr_b16 v[94:95], v160 offset:64
	ds_read_b64_tr_b16 v[96:97], v160 offset:1856
	s_waitcnt lgkmcnt(0)
	s_nop 0
	v_mfma_f32_16x16x32_f16 v[86:89], v[86:89], v[70:73], 0
	v_mfma_f32_16x16x32_f16 v[90:93], v[90:93], v[70:73], 0
	v_mfma_f32_16x16x32_f16 v[70:73], v[94:97], v[70:73], 0
	s_and_b64 vcc, exec, s[88:89]
	s_cbranch_vccz .LBB0_5150
	s_branch .LBB0_5151

.LBB0_5151:
	s_and_b64 vcc, exec, s[90:91]
	s_cbranch_vccnz .LBB0_5153
	s_waitcnt lgkmcnt(0)
	s_nop 0
	v_mfma_f32_16x16x32_f16 v[86:89], v[226:229], v[78:81], v[86:89]
	v_mfma_f32_16x16x32_f16 v[90:93], v[230:233], v[78:81], v[90:93]
	v_mfma_f32_16x16x32_f16 v[70:73], v[234:237], v[78:81], v[70:73]
	s_and_b64 vcc, exec, s[92:93]
	s_cbranch_vccz .LBB0_5154
	s_branch .LBB0_5155
